# MoE: rowmap gather-offset loads no longer drained at unit top (raw rows parked in spare VGPRs, converted inside K-loop); first K-iteration after an epilogue skips the two vmcnt waits that only guard p
# baseline (speedup 1.0000x reference)
.LBB0_2030:
	v_readlane_b32 s24, v253, 60
	v_readlane_b32 s25, v253, 61
	s_lshl_b64 s[22:23], s[24:25], 18
	s_waitcnt lgkmcnt(0)
	s_add_u32 s72, s20, s22
	s_addc_u32 s73, s21, s23
	v_lshrrev_b32_e32 v11, 1, v18
	s_add_u32 s20, s2, 0x67734900
	v_and_b32_e32 v11, 24, v11
	s_addc_u32 s21, s3, 0
	s_lshl_b64 s[2:3], s[24:25], 17
	v_and_b32_e32 v10, 15, v18
	v_lshlrev_b32_e32 v12, 1, v11
	s_add_u32 s74, s6, s2
	v_lshl_or_b32 v157, s0, 6, v10
	v_lshl_or_b32 v10, v10, 6, v12
	v_lshlrev_b32_e32 v12, 2, v18
	s_addc_u32 s75, s7, s3
	s_lshl_b32 s0, s0, 13
	v_and_b32_e32 v12, 32, v12
	v_bitop3_b32 v13, v10, s0, v12 bitop3:0xde
	s_lshl_b32 s0, s1, 5
	s_and_b32 s2, s0, 0x60
	s_add_i32 m0, s68, 0x18000
	v_lshl_add_u64 v[8:9], v[8:9], 0, s[46:47]
	s_lshl_b32 s0, s2, 7
	s_waitcnt vmcnt(2)
	s_barrier
	global_load_lds_dwordx4 v[8:9], off
	v_lshl_add_u64 v[6:7], v[6:7], 0, s[46:47]
	s_add_i32 m0, s68, 0x1a000
	s_add_i32 s76, s68, 0x8000
	s_add_i32 s77, s68, 0xa000
	v_bitop3_b32 v159, s0, v10, v12 bitop3:0xf6
	global_load_lds_dwordx4 v[6:7], off
	v_lshl_add_u64 v[2:3], v[2:3], 0, s[46:47]
	s_mov_b32 m0, s76
	s_add_u32 s0, s52, 0x40080
	global_load_lds_dwordx4 v[2:3], off
	v_lshl_add_u64 v[2:3], v[4:5], 0, s[46:47]
	s_mov_b32 m0, s77
	s_addc_u32 s1, s53, 0
	global_load_lds_dwordx4 v[2:3], off
	s_add_i32 m0, s68, 0x1c000
	v_lshl_add_u64 v[2:3], s[0:1], 0, v[150:151]
	global_load_lds_dwordx4 v[2:3], off
	v_lshl_add_u64 v[2:3], s[0:1], 0, v[152:153]
	s_add_i32 m0, s68, 0x1e000
	s_cmp_lt_u32 s31, 64
	global_load_lds_dwordx4 v[2:3], off
	s_cselect_b64 s[22:23], -1, 0
	s_cmpk_lt_u32 s31, 0x100
	v_readlane_b32 s36, v252, 29
	s_cselect_b64 s[24:25], -1, 0
	s_and_b32 s0, s30, 7
	s_ashr_i32 s1, s59, 3
	v_readlane_b32 s37, v252, 30
	s_mul_i32 s0, s1, s0
	s_ashr_i32 s1, s30, 3
	v_readlane_b32 s38, v252, 31
	v_readlane_b32 s39, v252, 32
	s_and_b32 s37, s66, 0xffff
	v_or_b32_e32 v178, s2, v11
	s_add_i32 s2, s0, s1
	s_lshl_b64 s[26:27], s[26:27], 2
	v_writelane_b32 v252, s36, 29
	s_waitcnt vmcnt(6)
	s_and_b64 s[0:1], s[28:29], exec
	s_cselect_b32 s78, s2, s30
	v_writelane_b32 v252, s37, 30
	v_writelane_b32 v252, s38, 31
	v_mov_b32_e32 v2, 0
	v_or_b32_e32 v179, 0xfffff800, v178
	s_mov_b32 s81, 0
	v_cmp_ne_u32_e64 s[6:7], 0, v0
	v_writelane_b32 v252, s39, 32
	s_ashr_i32 s79, s78, 31
	s_mov_b32 s50, -1
	v_add_u32_e32 v180, 0, v13
	v_mov_b32_e32 v3, v2
	v_mov_b32_e32 v4, v2
	v_mov_b32_e32 v5, v2
	v_mov_b32_e32 v6, v2
	v_mov_b32_e32 v7, v2
	v_mov_b32_e32 v8, v2
	v_mov_b32_e32 v9, v2
	v_mov_b32_e32 v10, v2
	v_mov_b32_e32 v11, v2
	v_mov_b32_e32 v12, v2
	v_mov_b32_e32 v13, v2
	v_mov_b32_e32 v14, v2
	v_mov_b32_e32 v15, v2
	v_mov_b32_e32 v16, v2
	v_mov_b32_e32 v17, v2
	v_mov_b32_e32 v18, v2
	v_mov_b32_e32 v19, v2
	v_mov_b32_e32 v20, v2
	v_mov_b32_e32 v21, v2
	v_mov_b32_e32 v22, v2
	v_mov_b32_e32 v23, v2
	v_mov_b32_e32 v24, v2
	v_mov_b32_e32 v25, v2
	v_mov_b32_e32 v26, v2
	v_mov_b32_e32 v27, v2
	v_mov_b32_e32 v28, v2
	v_mov_b32_e32 v29, v2
	v_mov_b32_e32 v30, v2
	v_mov_b32_e32 v31, v2
	v_mov_b32_e32 v32, v2
	v_mov_b32_e32 v33, v2
	v_mov_b32_e32 v38, v2
	v_mov_b32_e32 v39, v2
	v_mov_b32_e32 v40, v2
	v_mov_b32_e32 v41, v2
	v_mov_b32_e32 v42, v2
	v_mov_b32_e32 v43, v2
	v_mov_b32_e32 v44, v2
	v_mov_b32_e32 v45, v2
	v_mov_b32_e32 v46, v2
	v_mov_b32_e32 v47, v2
	v_mov_b32_e32 v48, v2
	v_mov_b32_e32 v49, v2
	v_mov_b32_e32 v50, v2
	v_mov_b32_e32 v51, v2
	v_mov_b32_e32 v52, v2
	v_mov_b32_e32 v53, v2
	v_mov_b32_e32 v54, v2
	v_mov_b32_e32 v55, v2
	v_mov_b32_e32 v56, v2
	v_mov_b32_e32 v57, v2
	v_mov_b32_e32 v58, v2
	v_mov_b32_e32 v59, v2
	v_mov_b32_e32 v60, v2
	v_mov_b32_e32 v61, v2
	v_mov_b32_e32 v62, v2
	v_mov_b32_e32 v63, v2
	v_mov_b32_e32 v64, v2
	v_mov_b32_e32 v65, v2
	v_mov_b32_e32 v66, v2
	v_mov_b32_e32 v67, v2
	v_mov_b32_e32 v68, v2
	v_mov_b32_e32 v69, v2
	v_mov_b32_e32 v70, v2
	v_mov_b32_e32 v71, v2
	v_mov_b32_e32 v72, v2
	v_mov_b32_e32 v73, v2
	v_mov_b32_e32 v74, v2
	v_mov_b32_e32 v75, v2
	v_mov_b32_e32 v76, v2
	v_mov_b32_e32 v77, v2
	v_mov_b32_e32 v78, v2
	v_mov_b32_e32 v79, v2
	v_mov_b32_e32 v80, v2
	v_mov_b32_e32 v81, v2
	v_mov_b32_e32 v82, v2
	v_mov_b32_e32 v83, v2
	v_mov_b32_e32 v84, v2
	v_mov_b32_e32 v85, v2
	v_mov_b32_e32 v86, v2
	v_mov_b32_e32 v87, v2
	v_mov_b32_e32 v88, v2
	v_mov_b32_e32 v89, v2
	v_mov_b32_e32 v90, v2
	v_mov_b32_e32 v91, v2
	v_mov_b32_e32 v92, v2
	v_mov_b32_e32 v93, v2
	v_mov_b32_e32 v94, v2
	v_mov_b32_e32 v95, v2
	v_mov_b32_e32 v96, v2
	v_mov_b32_e32 v97, v2
	v_mov_b32_e32 v98, v2
	v_mov_b32_e32 v99, v2
	v_mov_b32_e32 v100, v2
	v_mov_b32_e32 v101, v2
	v_mov_b32_e32 v102, v2
	v_mov_b32_e32 v103, v2
	v_mov_b32_e32 v104, v2
	v_mov_b32_e32 v105, v2
	v_mov_b32_e32 v106, v2
	v_mov_b32_e32 v107, v2
	v_mov_b32_e32 v108, v2
	v_mov_b32_e32 v109, v2
	v_mov_b32_e32 v110, v2
	v_mov_b32_e32 v111, v2
	v_mov_b32_e32 v112, v2
	v_mov_b32_e32 v113, v2
	v_mov_b32_e32 v114, v2
	v_mov_b32_e32 v115, v2
	v_mov_b32_e32 v116, v2
	v_mov_b32_e32 v117, v2
	v_mov_b32_e32 v118, v2
	v_mov_b32_e32 v119, v2
	v_mov_b32_e32 v120, v2
	v_mov_b32_e32 v121, v2
	v_mov_b32_e32 v122, v2
	v_mov_b32_e32 v123, v2
	v_mov_b32_e32 v124, v2
	v_mov_b32_e32 v125, v2
	v_mov_b32_e32 v126, v2
	v_mov_b32_e32 v127, v2
	v_mov_b32_e32 v128, v2
	v_mov_b32_e32 v129, v2
	v_mov_b32_e32 v130, v2
	v_mov_b32_e32 v131, v2
	v_mov_b32_e32 v132, v2
	v_mov_b32_e32 v133, v2
	s_barrier
	s_mov_b32 s32, 0

.LBB0_2042:
	v_cndmask_b32_e64 v0, 0, 1, s[42:43]
	v_cmp_ne_u32_e64 s[0:1], 1, v0
	s_andn2_b64 vcc, exec, s[42:43]
	v_mov_b32_e32 v187, v160
	v_mov_b32_e32 v181, v154
	v_mov_b32_e32 v186, v156
	v_mov_b32_e32 v188, v158
	v_lshrrev_b32_e32 v223, 11, v160
	v_lshrrev_b32_e32 v250, 11, v154
	v_lshrrev_b32_e32 v249, 11, v156
	v_lshrrev_b32_e32 v248, 11, v158
	s_cbranch_vccnz .LBB0_2060
	s_andn2_b64 vcc, exec, s[2:3]
	s_cbranch_vccnz .LBB0_2054
	s_andn2_b64 vcc, exec, s[22:23]
	s_cbranch_vccnz .LBB0_2053
	s_ashr_i32 s31, s30, 31
	s_lshl_b64 s[2:3], s[30:31], 2
	s_add_u32 s2, s14, s2
	s_addc_u32 s3, s15, s3
	s_mov_b32 s13, 0x1000001
	s_branch .LBB0_2047

.LBB0_2054:
	s_lshl_b32 s13, s30, 8
	v_add_u32_e32 v134, s13, v174
	v_add_u32_e32 v136, s13, v175
	s_bitset1_b32 s13, 7
	v_add_u32_e32 v138, s13, v174
	v_add_u32_e32 v140, s13, v175
	s_andn2_b64 vcc, exec, s[54:55]
	s_cbranch_vccnz .Lmoe_rows_direct
	v_ashrrev_i32_e32 v135, 31, v134
	v_lshl_add_u64 v[134:135], v[134:135], 2, s[16:17]
	global_load_dword v248, v[134:135], off
	v_ashrrev_i32_e32 v137, 31, v136
	v_lshl_add_u64 v[136:137], v[136:137], 2, s[16:17]
	global_load_dword v249, v[136:137], off
	v_ashrrev_i32_e32 v139, 31, v138
	v_lshl_add_u64 v[138:139], v[138:139], 2, s[16:17]
	global_load_dword v250, v[138:139], off
	v_ashrrev_i32_e32 v141, 31, v140
	v_lshl_add_u64 v[140:141], v[140:141], 2, s[16:17]
	global_load_dword v223, v[140:141], off
	s_branch .LBB0_2060
.Lmoe_rows_direct:
	v_mov_b32_e32 v248, v134
	v_mov_b32_e32 v249, v136
	v_mov_b32_e32 v250, v138
	v_mov_b32_e32 v223, v140

.LBB0_2063:
	s_or_b64 exec, exec, s[50:51]
	s_add_i32 s33, s52, 0x180
	s_cmpk_eq_i32 s52, 0x700
	s_cselect_b64 s[40:41], -1, 0
	s_and_b64 s[40:41], s[40:41], exec
	s_cselect_b32 s56, 0x80, s33
	s_add_u32 s50, s52, 0x100
	s_addc_u32 s51, s53, 0
	s_cmpk_eq_i32 s52, 0x700
	s_cselect_b64 s[40:41], -1, 0
	s_and_b64 s[40:41], s[40:41], exec
	s_cselect_b32 s40, 0, s50
	s_add_u32 s33, s29, s52
	s_addc_u32 s41, s31, s53
	s_cmpk_eq_i32 s52, 0x700
	s_cselect_b64 vcc, -1, 0
	s_and_b64 s[46:47], vcc, exec
	s_cselect_b32 s54, s38, s33
	s_cselect_b32 s55, s39, s41
	s_add_i32 s33, 0, 0x10000
	v_add_u32_e32 v0, s33, v159
	s_add_i32 s41, 0, 0x14000
	ds_read_b128 v[140:143], v0
	ds_read_b128 v[144:147], v0 offset:1024
	ds_read_b128 v[162:165], v0 offset:2048
	ds_read_b128 v[166:169], v0 offset:3072
	v_add_u32_e32 v0, s41, v159
	ds_read_b128 v[170:173], v0
	ds_read_b128 v[190:193], v0 offset:1024
	ds_read_b128 v[194:197], v0 offset:2048
	ds_read_b128 v[198:201], v0 offset:3072
	v_lshl_add_u64 v[148:149], v[136:137], 0, s[52:53]
	s_add_i32 m0, s68, 0xc000
	ds_read_b128 v[224:227], v180
	ds_read_b128 v[228:231], v180 offset:1024
	ds_read_b128 v[232:235], v180 offset:2048
	ds_read_b128 v[236:239], v180 offset:3072
	ds_read_b128 v[240:243], v180 offset:4096
	ds_read_b128 v[244:247], v180 offset:5120
	ds_read_b128 v[182:185], v180 offset:6144
	ds_read_b128 v[218:221], v180 offset:7168
	global_load_lds_dwordx4 v[148:149], off
	v_lshl_add_u64 v[148:149], v[134:135], 0, s[52:53]
	s_add_i32 m0, s68, 0xe000
	s_nop 0
	global_load_lds_dwordx4 v[148:149], off
	s_cmp_lg_u32 s52, 0
	s_cbranch_scc1 .Lmw8_0
	s_cmp_lg_u32 s32, 0
	s_cbranch_scc1 .Lmwd_0
.Lmw8_0:
	s_waitcnt vmcnt(8)
.Lmwd_0:
	s_waitcnt lgkmcnt(0)
	s_barrier
	s_setprio 1
	s_waitcnt lgkmcnt(0)
	v_mfma_f32_16x16x32_bf16 v[130:133], v[140:143], v[224:227], v[130:133]
	v_mfma_f32_16x16x32_bf16 v[126:129], v[162:165], v[224:227], v[126:129]
	v_mfma_f32_16x16x32_bf16 v[122:125], v[140:143], v[232:235], v[122:125]
	v_mfma_f32_16x16x32_bf16 v[118:121], v[162:165], v[232:235], v[118:121]
	v_mfma_f32_16x16x32_bf16 v[114:117], v[140:143], v[240:243], v[114:117]
	v_mfma_f32_16x16x32_bf16 v[110:113], v[162:165], v[240:243], v[110:113]
	v_mfma_f32_16x16x32_bf16 v[106:109], v[140:143], v[182:185], v[106:109]
	v_mfma_f32_16x16x32_bf16 v[102:105], v[162:165], v[182:185], v[102:105]
	v_mfma_f32_16x16x32_bf16 v[130:133], v[144:147], v[228:231], v[130:133]
	v_mfma_f32_16x16x32_bf16 v[126:129], v[166:169], v[228:231], v[126:129]
	v_mfma_f32_16x16x32_bf16 v[122:125], v[144:147], v[236:239], v[122:125]
	v_mfma_f32_16x16x32_bf16 v[118:121], v[166:169], v[236:239], v[118:121]
	v_mfma_f32_16x16x32_bf16 v[114:117], v[144:147], v[244:247], v[114:117]
	v_mfma_f32_16x16x32_bf16 v[110:113], v[166:169], v[244:247], v[110:113]
	v_mfma_f32_16x16x32_bf16 v[106:109], v[144:147], v[218:221], v[106:109]
	v_mfma_f32_16x16x32_bf16 v[102:105], v[166:169], v[218:221], v[102:105]
	s_setprio 0
	s_setprio 1
	v_mfma_f32_16x16x32_bf16 v[98:101], v[170:173], v[224:227], v[98:101]
	v_mfma_f32_16x16x32_bf16 v[94:97], v[194:197], v[224:227], v[94:97]
	v_mfma_f32_16x16x32_bf16 v[90:93], v[170:173], v[232:235], v[90:93]
	v_mfma_f32_16x16x32_bf16 v[86:89], v[194:197], v[232:235], v[86:89]
	v_mfma_f32_16x16x32_bf16 v[82:85], v[170:173], v[240:243], v[82:85]
	v_mfma_f32_16x16x32_bf16 v[78:81], v[194:197], v[240:243], v[78:81]
	v_mfma_f32_16x16x32_bf16 v[74:77], v[170:173], v[182:185], v[74:77]
	v_mfma_f32_16x16x32_bf16 v[70:73], v[194:197], v[182:185], v[70:73]
	v_mfma_f32_16x16x32_bf16 v[98:101], v[190:193], v[228:231], v[98:101]
	v_mfma_f32_16x16x32_bf16 v[94:97], v[198:201], v[228:231], v[94:97]
	v_mfma_f32_16x16x32_bf16 v[90:93], v[190:193], v[236:239], v[90:93]
	v_mfma_f32_16x16x32_bf16 v[86:89], v[198:201], v[236:239], v[86:89]
	v_mfma_f32_16x16x32_bf16 v[82:85], v[190:193], v[244:247], v[82:85]
	v_mfma_f32_16x16x32_bf16 v[78:81], v[198:201], v[244:247], v[78:81]
	v_mfma_f32_16x16x32_bf16 v[74:77], v[190:193], v[218:221], v[74:77]
	v_mfma_f32_16x16x32_bf16 v[70:73], v[198:201], v[218:221], v[70:73]
	s_setprio 0
	s_barrier
	s_add_i32 s33, s33, s67
	v_lshl_add_u64 v[148:149], s[54:55], 0, v[150:151]
	s_mov_b32 m0, s33
	ds_read_b128 v[182:185], v180 offset:16384
	ds_read_b128 v[218:221], v180 offset:17408
	ds_read_b128 v[224:227], v180 offset:18432
	ds_read_b128 v[228:231], v180 offset:19456
	ds_read_b128 v[232:235], v180 offset:20480
	ds_read_b128 v[236:239], v180 offset:21504
	ds_read_b128 v[240:243], v180 offset:22528
	ds_read_b128 v[244:247], v180 offset:23552
	global_load_lds_dwordx4 v[148:149], off
	s_add_i32 m0, s33, 0x2000
	s_add_u32 s46, s54, 0x40000
	v_lshl_add_u64 v[202:203], s[54:55], 0, v[152:153]
	s_addc_u32 s47, s55, 0
	s_add_i32 s33, s41, s67
	global_load_lds_dwordx4 v[202:203], off
	v_lshl_add_u64 v[210:211], s[46:47], 0, v[150:151]
	s_mov_b32 m0, s33
	v_cndmask_b32_e32 v0, v158, v188, vcc
	global_load_lds_dwordx4 v[210:211], off
	v_lshl_add_u64 v[210:211], s[46:47], 0, v[152:153]
	s_add_i32 m0, s33, 0x2000
	s_and_b64 s[46:47], s[42:43], vcc
	s_and_b64 s[46:47], s[46:47], exec
	s_cselect_b32 s44, s2, s34
	s_cselect_b32 s33, s3, s35
	s_add_u32 s40, s44, s40
	global_load_lds_dwordx4 v[210:211], off
	s_addc_u32 s41, s33, 0
	s_mov_b32 m0, s68
	v_cndmask_b32_e32 v139, v156, v186, vcc
	global_load_lds_dwordx4 v0, s[40:41]
	s_mov_b32 m0, s69
	s_nop 0
	global_load_lds_dwordx4 v139, s[40:41]
	s_cmp_lg_u32 s52, 0
	s_cbranch_scc1 .Lmw8_1
	s_cmp_lg_u32 s32, 0
	s_cbranch_scc1 .Lmwd_1

.Lmwd_1:
	s_waitcnt lgkmcnt(0)
	s_barrier
	s_setprio 1
	s_waitcnt lgkmcnt(0)
	v_mfma_f32_16x16x32_bf16 v[66:69], v[140:143], v[182:185], v[66:69]
	v_mfma_f32_16x16x32_bf16 v[62:65], v[162:165], v[182:185], v[62:65]
	v_mfma_f32_16x16x32_bf16 v[58:61], v[140:143], v[224:227], v[58:61]
	v_mfma_f32_16x16x32_bf16 v[54:57], v[162:165], v[224:227], v[54:57]
	v_mfma_f32_16x16x32_bf16 v[50:53], v[140:143], v[232:235], v[50:53]
	v_mfma_f32_16x16x32_bf16 v[46:49], v[162:165], v[232:235], v[46:49]
	v_mfma_f32_16x16x32_bf16 v[42:45], v[140:143], v[240:243], v[42:45]
	v_mfma_f32_16x16x32_bf16 v[38:41], v[162:165], v[240:243], v[38:41]
	v_mfma_f32_16x16x32_bf16 v[66:69], v[144:147], v[218:221], v[66:69]
	v_mfma_f32_16x16x32_bf16 v[62:65], v[166:169], v[218:221], v[62:65]
	v_mfma_f32_16x16x32_bf16 v[58:61], v[144:147], v[228:231], v[58:61]
	v_mfma_f32_16x16x32_bf16 v[54:57], v[166:169], v[228:231], v[54:57]
	v_mfma_f32_16x16x32_bf16 v[50:53], v[144:147], v[236:239], v[50:53]
	v_mfma_f32_16x16x32_bf16 v[46:49], v[166:169], v[236:239], v[46:49]
	v_mfma_f32_16x16x32_bf16 v[42:45], v[144:147], v[244:247], v[42:45]
	v_mfma_f32_16x16x32_bf16 v[38:41], v[166:169], v[244:247], v[38:41]
	s_setprio 0
	s_setprio 1
	v_mfma_f32_16x16x32_bf16 v[30:33], v[170:173], v[182:185], v[30:33]
	v_mfma_f32_16x16x32_bf16 v[26:29], v[194:197], v[182:185], v[26:29]
	v_mfma_f32_16x16x32_bf16 v[22:25], v[170:173], v[224:227], v[22:25]
	v_mfma_f32_16x16x32_bf16 v[18:21], v[194:197], v[224:227], v[18:21]
	v_mfma_f32_16x16x32_bf16 v[14:17], v[170:173], v[232:235], v[14:17]
	v_mfma_f32_16x16x32_bf16 v[10:13], v[194:197], v[232:235], v[10:13]
	v_mfma_f32_16x16x32_bf16 v[6:9], v[170:173], v[240:243], v[6:9]
	v_mfma_f32_16x16x32_bf16 v[2:5], v[194:197], v[240:243], v[2:5]
	v_mfma_f32_16x16x32_bf16 v[30:33], v[190:193], v[218:221], v[30:33]
	v_mfma_f32_16x16x32_bf16 v[26:29], v[198:201], v[218:221], v[26:29]
	v_mfma_f32_16x16x32_bf16 v[22:25], v[190:193], v[228:231], v[22:25]
	v_mfma_f32_16x16x32_bf16 v[18:21], v[198:201], v[228:231], v[18:21]
	v_mfma_f32_16x16x32_bf16 v[14:17], v[190:193], v[236:239], v[14:17]
	v_mfma_f32_16x16x32_bf16 v[10:13], v[198:201], v[236:239], v[10:13]
	v_mfma_f32_16x16x32_bf16 v[6:9], v[190:193], v[244:247], v[6:9]
	v_mfma_f32_16x16x32_bf16 v[2:5], v[198:201], v[244:247], v[2:5]
	s_setprio 0
	s_barrier
	s_add_i32 s46, 0, 0x18000
	v_add_u32_e32 v155, s46, v159
	s_add_i32 s47, 0, 0x1c000
	ds_read_b128 v[140:143], v155
	ds_read_b128 v[144:147], v155 offset:1024
	ds_read_b128 v[162:165], v155 offset:2048
	ds_read_b128 v[166:169], v155 offset:3072
	v_add_u32_e32 v155, s47, v159
	ds_read_b128 v[170:173], v155
	ds_read_b128 v[182:185], v155 offset:1024
	ds_read_b128 v[190:193], v155 offset:2048
	ds_read_b128 v[194:197], v155 offset:3072
	s_mov_b32 m0, s70
	v_cndmask_b32_e32 v155, v154, v181, vcc
	ds_read_b128 v[198:201], v180 offset:32768
	ds_read_b128 v[218:221], v180 offset:33792
	ds_read_b128 v[224:227], v180 offset:34816
	ds_read_b128 v[228:231], v180 offset:35840
	ds_read_b128 v[232:235], v180 offset:36864
	ds_read_b128 v[236:239], v180 offset:37888
	ds_read_b128 v[240:243], v180 offset:38912
	ds_read_b128 v[244:247], v180 offset:39936
	global_load_lds_dwordx4 v155, s[40:41]
	v_cndmask_b32_e32 v155, v160, v187, vcc
	s_mov_b32 m0, s71
	s_nop 0
	global_load_lds_dwordx4 v155, s[40:41]
	s_waitcnt vmcnt(8)
	s_waitcnt lgkmcnt(0)
	s_barrier
	s_setprio 1
	s_waitcnt lgkmcnt(0)
	v_mfma_f32_16x16x32_bf16 v[130:133], v[140:143], v[198:201], v[130:133]
	v_mfma_f32_16x16x32_bf16 v[126:129], v[162:165], v[198:201], v[126:129]
	v_mfma_f32_16x16x32_bf16 v[122:125], v[140:143], v[224:227], v[122:125]
	v_mfma_f32_16x16x32_bf16 v[118:121], v[162:165], v[224:227], v[118:121]
	v_mfma_f32_16x16x32_bf16 v[114:117], v[140:143], v[232:235], v[114:117]
	v_mfma_f32_16x16x32_bf16 v[110:113], v[162:165], v[232:235], v[110:113]
	v_mfma_f32_16x16x32_bf16 v[106:109], v[140:143], v[240:243], v[106:109]
	v_mfma_f32_16x16x32_bf16 v[102:105], v[162:165], v[240:243], v[102:105]
	v_mfma_f32_16x16x32_bf16 v[130:133], v[144:147], v[218:221], v[130:133]
	v_mfma_f32_16x16x32_bf16 v[126:129], v[166:169], v[218:221], v[126:129]
	v_mfma_f32_16x16x32_bf16 v[122:125], v[144:147], v[228:231], v[122:125]
	v_mfma_f32_16x16x32_bf16 v[118:121], v[166:169], v[228:231], v[118:121]
	v_mfma_f32_16x16x32_bf16 v[114:117], v[144:147], v[236:239], v[114:117]
	v_mfma_f32_16x16x32_bf16 v[110:113], v[166:169], v[236:239], v[110:113]
	v_mfma_f32_16x16x32_bf16 v[106:109], v[144:147], v[244:247], v[106:109]
	v_mfma_f32_16x16x32_bf16 v[102:105], v[166:169], v[244:247], v[102:105]
	s_setprio 0
	s_setprio 1
	v_mfma_f32_16x16x32_bf16 v[98:101], v[170:173], v[198:201], v[98:101]
	v_mfma_f32_16x16x32_bf16 v[94:97], v[190:193], v[198:201], v[94:97]
	v_mfma_f32_16x16x32_bf16 v[90:93], v[170:173], v[224:227], v[90:93]
	v_mfma_f32_16x16x32_bf16 v[86:89], v[190:193], v[224:227], v[86:89]
	v_mfma_f32_16x16x32_bf16 v[82:85], v[170:173], v[232:235], v[82:85]
	v_mfma_f32_16x16x32_bf16 v[78:81], v[190:193], v[232:235], v[78:81]
	v_mfma_f32_16x16x32_bf16 v[74:77], v[170:173], v[240:243], v[74:77]
	v_mfma_f32_16x16x32_bf16 v[70:73], v[190:193], v[240:243], v[70:73]
	v_mfma_f32_16x16x32_bf16 v[98:101], v[182:185], v[218:221], v[98:101]
	v_mfma_f32_16x16x32_bf16 v[94:97], v[194:197], v[218:221], v[94:97]
	v_mfma_f32_16x16x32_bf16 v[90:93], v[182:185], v[228:231], v[90:93]
	v_mfma_f32_16x16x32_bf16 v[86:89], v[194:197], v[228:231], v[86:89]
	v_mfma_f32_16x16x32_bf16 v[82:85], v[182:185], v[236:239], v[82:85]
	v_mfma_f32_16x16x32_bf16 v[78:81], v[194:197], v[236:239], v[78:81]
	v_mfma_f32_16x16x32_bf16 v[74:77], v[182:185], v[244:247], v[74:77]
	v_mfma_f32_16x16x32_bf16 v[70:73], v[194:197], v[244:247], v[70:73]
	s_setprio 0
	s_barrier
	s_mov_b64 s[52:53], 0x80
	s_add_i32 s40, s46, s67
	v_lshl_add_u64 v[148:149], v[148:149], 0, s[52:53]
	s_mov_b32 m0, s40
	ds_read_b128 v[198:201], v180 offset:49152
	ds_read_b128 v[218:221], v180 offset:50176
	ds_read_b128 v[224:227], v180 offset:51200
	ds_read_b128 v[228:231], v180 offset:52224
	ds_read_b128 v[232:235], v180 offset:53248
	ds_read_b128 v[236:239], v180 offset:54272
	ds_read_b128 v[240:243], v180 offset:55296
	ds_read_b128 v[244:247], v180 offset:56320
	global_load_lds_dwordx4 v[148:149], off
	s_add_i32 m0, s40, 0x2000
	s_add_u32 s40, s54, 0x40080
	v_lshl_add_u64 v[148:149], v[202:203], 0, s[52:53]
	s_addc_u32 s41, s55, 0
	s_add_i32 s46, s47, s67
	global_load_lds_dwordx4 v[148:149], off
	v_lshl_add_u64 v[148:149], s[40:41], 0, v[150:151]
	s_mov_b32 m0, s46
	s_nop 0
	global_load_lds_dwordx4 v[148:149], off
	s_add_i32 m0, s46, 0x2000
	v_lshl_add_u64 v[148:149], s[40:41], 0, v[152:153]
	s_add_u32 s40, s44, s56
	global_load_lds_dwordx4 v[148:149], off
	s_addc_u32 s41, s33, 0
	s_mov_b32 m0, s76
	s_nop 0
	global_load_lds_dwordx4 v0, s[40:41]
	s_mov_b32 m0, s77
	s_nop 0
	global_load_lds_dwordx4 v139, s[40:41]
	s_waitcnt vmcnt(8)
	v_lshl_add_u32 v181, v250, 11, v176
	v_lshl_add_u32 v186, v249, 11, v177
	v_lshl_add_u32 v188, v248, 11, v176
	v_lshl_add_u32 v187, v223, 11, v177
	s_waitcnt lgkmcnt(0)
	s_barrier
	s_setprio 1
	s_waitcnt lgkmcnt(0)
	v_mfma_f32_16x16x32_bf16 v[66:69], v[140:143], v[198:201], v[66:69]
	v_mfma_f32_16x16x32_bf16 v[62:65], v[162:165], v[198:201], v[62:65]
	v_mfma_f32_16x16x32_bf16 v[58:61], v[140:143], v[224:227], v[58:61]
	v_mfma_f32_16x16x32_bf16 v[54:57], v[162:165], v[224:227], v[54:57]
	v_mfma_f32_16x16x32_bf16 v[50:53], v[140:143], v[232:235], v[50:53]
	v_mfma_f32_16x16x32_bf16 v[46:49], v[162:165], v[232:235], v[46:49]
	v_mfma_f32_16x16x32_bf16 v[42:45], v[140:143], v[240:243], v[42:45]
	v_mfma_f32_16x16x32_bf16 v[38:41], v[162:165], v[240:243], v[38:41]
	v_mfma_f32_16x16x32_bf16 v[66:69], v[144:147], v[218:221], v[66:69]
	v_mfma_f32_16x16x32_bf16 v[62:65], v[166:169], v[218:221], v[62:65]
	v_mfma_f32_16x16x32_bf16 v[58:61], v[144:147], v[228:231], v[58:61]
	v_mfma_f32_16x16x32_bf16 v[54:57], v[166:169], v[228:231], v[54:57]
	v_mfma_f32_16x16x32_bf16 v[50:53], v[144:147], v[236:239], v[50:53]
	v_mfma_f32_16x16x32_bf16 v[46:49], v[166:169], v[236:239], v[46:49]
	v_mfma_f32_16x16x32_bf16 v[42:45], v[144:147], v[244:247], v[42:45]
	v_mfma_f32_16x16x32_bf16 v[38:41], v[166:169], v[244:247], v[38:41]
	s_setprio 0
	s_setprio 1
	v_mfma_f32_16x16x32_bf16 v[30:33], v[170:173], v[198:201], v[30:33]
	v_mfma_f32_16x16x32_bf16 v[26:29], v[190:193], v[198:201], v[26:29]
	v_mfma_f32_16x16x32_bf16 v[22:25], v[170:173], v[224:227], v[22:25]
	v_mfma_f32_16x16x32_bf16 v[18:21], v[190:193], v[224:227], v[18:21]
	v_mfma_f32_16x16x32_bf16 v[14:17], v[170:173], v[232:235], v[14:17]
	v_mfma_f32_16x16x32_bf16 v[10:13], v[190:193], v[232:235], v[10:13]
	v_mfma_f32_16x16x32_bf16 v[6:9], v[170:173], v[240:243], v[6:9]
	v_mfma_f32_16x16x32_bf16 v[2:5], v[190:193], v[240:243], v[2:5]
	v_mfma_f32_16x16x32_bf16 v[30:33], v[182:185], v[218:221], v[30:33]
	v_mfma_f32_16x16x32_bf16 v[26:29], v[194:197], v[218:221], v[26:29]
	v_mfma_f32_16x16x32_bf16 v[22:25], v[182:185], v[228:231], v[22:25]
	v_mfma_f32_16x16x32_bf16 v[18:21], v[194:197], v[228:231], v[18:21]
	v_mfma_f32_16x16x32_bf16 v[14:17], v[182:185], v[236:239], v[14:17]
	v_mfma_f32_16x16x32_bf16 v[10:13], v[194:197], v[236:239], v[10:13]
	v_mfma_f32_16x16x32_bf16 v[6:9], v[182:185], v[244:247], v[6:9]
	v_mfma_f32_16x16x32_bf16 v[2:5], v[194:197], v[244:247], v[2:5]
	s_setprio 0
	s_barrier
	s_add_i32 s13, s13, 2
	s_cmp_gt_u32 s13, 13
	s_cbranch_scc1 .LBB0_2065
	s_mov_b64 s[52:53], s[50:51]
	v_mov_b32_e32 v0, v138
	s_branch .LBB0_2061

.LBB0_2073:
	s_mov_b32 s32, 1
	s_lshl_b64 s[40:41], s[12:13], 12
	s_add_u32 s40, s74, s40
	v_lshl_add_u32 v0, s60, 8, v179
	s_addc_u32 s41, s75, s41
	v_lshl_add_u64 v[138:139], v[0:1], 2, s[40:41]
	global_load_dwordx4 v[142:145], v[138:139], off offset:16
	global_load_dwordx4 v[146:149], v[138:139], off
	global_load_dwordx4 v[134:137], v[138:139], off offset:528
	s_nop 0
	global_load_dwordx4 v[138:141], v[138:139], off offset:512
	v_ashrrev_i32_e32 v163, 31, v162
	v_lshlrev_b64 v[164:165], 11, v[162:163]
	v_lshl_add_u64 v[164:165], s[20:21], 0, v[164:165]
	v_lshlrev_b64 v[166:167], 1, v[0:1]
	v_lshl_add_u64 v[164:165], v[164:165], 0, v[166:167]
	s_mov_b32 s33, 0x40000
	s_mov_b64 s[40:41], 0x40000
	s_waitcnt vmcnt(0)
	v_pk_add_f32 v[172:173], v[128:129], v[144:145]
	v_pk_add_f32 v[170:171], v[132:133], v[148:149]
	v_pk_add_f32 v[168:169], v[130:131], v[146:147]
	v_pk_add_f32 v[182:183], v[126:127], v[142:143]
	v_cvt_pk_bf16_f32 v168, v168, v169
	v_cvt_pk_bf16_f32 v169, v170, v171
	v_cvt_pk_bf16_f32 v170, v182, v183
	v_cvt_pk_bf16_f32 v171, v172, v173
	global_store_dwordx4 v[164:165], v[168:171], off
	v_pk_add_f32 v[172:173], v[96:97], v[136:137]
	v_pk_add_f32 v[182:183], v[94:95], v[134:135]
	v_pk_add_f32 v[170:171], v[100:101], v[140:141]
	v_pk_add_f32 v[168:169], v[98:99], v[138:139]
	v_pk_add_f32 v[184:185], v[118:119], v[142:143]
	v_cvt_pk_bf16_f32 v168, v168, v169
	v_cvt_pk_bf16_f32 v169, v170, v171
	v_cvt_pk_bf16_f32 v170, v182, v183
	v_cvt_pk_bf16_f32 v171, v172, v173
	global_store_dwordx4 v[164:165], v[168:171], off offset:256
	v_pk_add_f32 v[182:183], v[120:121], v[144:145]
	s_nop 0
	v_or_b32_e32 v168, 16, v162
	v_ashrrev_i32_e32 v169, 31, v168
	v_lshlrev_b64 v[168:169], 11, v[168:169]
	v_lshl_add_u64 v[168:169], s[20:21], 0, v[168:169]
	v_lshl_add_u64 v[172:173], v[168:169], 0, v[166:167]
	v_pk_add_f32 v[170:171], v[124:125], v[148:149]
	v_pk_add_f32 v[168:169], v[122:123], v[146:147]
	s_nop 0
	v_cvt_pk_bf16_f32 v168, v168, v169
	v_cvt_pk_bf16_f32 v169, v170, v171
	v_cvt_pk_bf16_f32 v170, v184, v185
	v_cvt_pk_bf16_f32 v171, v182, v183
	global_store_dwordx4 v[172:173], v[168:171], off
	v_pk_add_f32 v[182:183], v[88:89], v[136:137]
	v_pk_add_f32 v[184:185], v[86:87], v[134:135]
	v_pk_add_f32 v[170:171], v[92:93], v[140:141]
	v_pk_add_f32 v[168:169], v[90:91], v[138:139]
	s_nop 0
	v_cvt_pk_bf16_f32 v168, v168, v169
	v_cvt_pk_bf16_f32 v169, v170, v171
	v_cvt_pk_bf16_f32 v170, v184, v185
	v_cvt_pk_bf16_f32 v171, v182, v183
	global_store_dwordx4 v[172:173], v[168:171], off offset:256
	v_pk_add_f32 v[182:183], v[112:113], v[144:145]
	v_pk_add_f32 v[184:185], v[110:111], v[142:143]
	v_or_b32_e32 v168, 32, v162
	v_ashrrev_i32_e32 v169, 31, v168
	v_lshlrev_b64 v[168:169], 11, v[168:169]
	v_lshl_add_u64 v[168:169], s[20:21], 0, v[168:169]
	v_lshl_add_u64 v[172:173], v[168:169], 0, v[166:167]
	v_pk_add_f32 v[170:171], v[116:117], v[148:149]
	v_pk_add_f32 v[168:169], v[114:115], v[146:147]
	s_nop 0
	v_cvt_pk_bf16_f32 v168, v168, v169
	v_cvt_pk_bf16_f32 v169, v170, v171
	v_cvt_pk_bf16_f32 v170, v184, v185
	v_cvt_pk_bf16_f32 v171, v182, v183
	global_store_dwordx4 v[172:173], v[168:171], off
	v_pk_add_f32 v[182:183], v[80:81], v[136:137]
	v_pk_add_f32 v[184:185], v[78:79], v[134:135]
	v_pk_add_f32 v[170:171], v[84:85], v[140:141]
	v_pk_add_f32 v[168:169], v[82:83], v[138:139]
	s_nop 0
	v_cvt_pk_bf16_f32 v168, v168, v169
	v_cvt_pk_bf16_f32 v169, v170, v171
	v_cvt_pk_bf16_f32 v170, v184, v185
	v_cvt_pk_bf16_f32 v171, v182, v183
	global_store_dwordx4 v[172:173], v[168:171], off offset:256
	v_pk_add_f32 v[172:173], v[104:105], v[144:145]
	v_pk_add_f32 v[182:183], v[102:103], v[142:143]
	v_or_b32_e32 v168, 48, v162
	v_ashrrev_i32_e32 v169, 31, v168
	v_lshlrev_b64 v[168:169], 11, v[168:169]
	v_lshl_add_u64 v[168:169], s[20:21], 0, v[168:169]
	v_lshl_add_u64 v[170:171], v[168:169], 0, v[166:167]
	v_pk_add_f32 v[168:169], v[108:109], v[148:149]
	v_pk_add_f32 v[166:167], v[106:107], v[146:147]
	s_nop 0
	v_cvt_pk_bf16_f32 v166, v166, v167
	v_cvt_pk_bf16_f32 v167, v168, v169
	v_cvt_pk_bf16_f32 v168, v182, v183
	v_cvt_pk_bf16_f32 v169, v172, v173
	global_store_dwordx4 v[170:171], v[166:169], off
	v_pk_add_f32 v[172:173], v[72:73], v[136:137]
	v_pk_add_f32 v[182:183], v[70:71], v[134:135]
	v_pk_add_f32 v[168:169], v[76:77], v[140:141]
	v_pk_add_f32 v[166:167], v[74:75], v[138:139]
	s_nop 0
	v_cvt_pk_bf16_f32 v166, v166, v167
	v_cvt_pk_bf16_f32 v167, v168, v169
	v_cvt_pk_bf16_f32 v168, v182, v183
	v_cvt_pk_bf16_f32 v169, v172, v173
	global_store_dwordx4 v[170:171], v[166:169], off offset:256
	v_pk_add_f32 v[172:173], v[64:65], v[144:145]
	v_pk_add_f32 v[182:183], v[62:63], v[142:143]
	v_pk_add_f32 v[168:169], v[68:69], v[148:149]
	v_pk_add_f32 v[166:167], v[66:67], v[146:147]
	v_lshl_add_u64 v[170:171], v[164:165], 0, s[40:41]
	v_cvt_pk_bf16_f32 v166, v166, v167
	v_cvt_pk_bf16_f32 v167, v168, v169
	v_cvt_pk_bf16_f32 v169, v172, v173
	v_add_co_u32_e32 v172, vcc, s33, v164
	v_cvt_pk_bf16_f32 v168, v182, v183
	s_nop 0
	v_addc_co_u32_e32 v173, vcc, 0, v165, vcc
	global_store_dwordx4 v[172:173], v[166:169], off
	v_pk_add_f32 v[172:173], v[28:29], v[136:137]
	v_pk_add_f32 v[182:183], v[26:27], v[134:135]
	v_pk_add_f32 v[168:169], v[32:33], v[140:141]
	v_pk_add_f32 v[166:167], v[30:31], v[138:139]
	s_mov_b32 s33, 0x48000
	v_cvt_pk_bf16_f32 v166, v166, v167
	v_cvt_pk_bf16_f32 v167, v168, v169
	v_cvt_pk_bf16_f32 v168, v182, v183
	v_cvt_pk_bf16_f32 v169, v172, v173
	global_store_dwordx4 v[170:171], v[166:169], off offset:256
	v_pk_add_f32 v[172:173], v[56:57], v[144:145]
	v_pk_add_f32 v[182:183], v[54:55], v[142:143]
	v_pk_add_f32 v[168:169], v[60:61], v[148:149]
	v_pk_add_f32 v[166:167], v[58:59], v[146:147]
	s_mov_b64 s[40:41], 0x48000
	v_cvt_pk_bf16_f32 v166, v166, v167
	v_cvt_pk_bf16_f32 v167, v168, v169
	v_cvt_pk_bf16_f32 v169, v172, v173
	v_add_co_u32_e32 v172, vcc, s33, v164
	v_cvt_pk_bf16_f32 v168, v182, v183
	s_nop 0
	v_addc_co_u32_e32 v173, vcc, 0, v165, vcc
	global_store_dwordx4 v[172:173], v[166:169], off
	v_pk_add_f32 v[172:173], v[20:21], v[136:137]
	v_pk_add_f32 v[182:183], v[18:19], v[134:135]
	v_pk_add_f32 v[168:169], v[24:25], v[140:141]
	v_pk_add_f32 v[166:167], v[22:23], v[138:139]
	v_lshl_add_u64 v[170:171], v[164:165], 0, s[40:41]
	v_cvt_pk_bf16_f32 v166, v166, v167
	v_cvt_pk_bf16_f32 v167, v168, v169
	v_cvt_pk_bf16_f32 v168, v182, v183
	v_cvt_pk_bf16_f32 v169, v172, v173
	global_store_dwordx4 v[170:171], v[166:169], off offset:256
	v_pk_add_f32 v[172:173], v[48:49], v[144:145]
	s_mov_b32 s33, 0x50000
	v_pk_add_f32 v[168:169], v[52:53], v[148:149]
	v_pk_add_f32 v[166:167], v[50:51], v[146:147]
	v_pk_add_f32 v[182:183], v[46:47], v[142:143]
	v_cvt_pk_bf16_f32 v166, v166, v167
	v_cvt_pk_bf16_f32 v167, v168, v169
	v_cvt_pk_bf16_f32 v169, v172, v173
	v_add_co_u32_e32 v172, vcc, s33, v164
	v_cvt_pk_bf16_f32 v168, v182, v183
	s_nop 0
	v_addc_co_u32_e32 v173, vcc, 0, v165, vcc
	s_mov_b64 s[40:41], 0x50000
	global_store_dwordx4 v[172:173], v[166:169], off
	v_pk_add_f32 v[172:173], v[12:13], v[136:137]
	v_pk_add_f32 v[182:183], v[10:11], v[134:135]
	v_pk_add_f32 v[168:169], v[16:17], v[140:141]
	v_pk_add_f32 v[166:167], v[14:15], v[138:139]
	v_lshl_add_u64 v[170:171], v[164:165], 0, s[40:41]
	v_cvt_pk_bf16_f32 v166, v166, v167
	v_cvt_pk_bf16_f32 v167, v168, v169
	v_cvt_pk_bf16_f32 v168, v182, v183
	v_cvt_pk_bf16_f32 v169, v172, v173
	v_pk_add_f32 v[146:147], v[42:43], v[146:147]
	s_mov_b32 s33, 0x58000
	global_store_dwordx4 v[170:171], v[166:169], off offset:256
	v_pk_add_f32 v[148:149], v[44:45], v[148:149]
	s_mov_b64 s[40:41], 0x58000
	v_pk_add_f32 v[168:169], v[40:41], v[144:145]
	v_pk_add_f32 v[144:145], v[38:39], v[142:143]
	v_cvt_pk_bf16_f32 v142, v146, v147
	v_add_co_u32_e32 v146, vcc, s33, v164
	v_cvt_pk_bf16_f32 v143, v148, v149
	v_cvt_pk_bf16_f32 v144, v144, v145
	v_cvt_pk_bf16_f32 v145, v168, v169
	v_addc_co_u32_e32 v147, vcc, 0, v165, vcc
	global_store_dwordx4 v[146:147], v[142:145], off
	v_pk_add_f32 v[140:141], v[8:9], v[140:141]
	v_pk_add_f32 v[138:139], v[6:7], v[138:139]
	v_pk_add_f32 v[142:143], v[4:5], v[136:137]
	v_pk_add_f32 v[136:137], v[2:3], v[134:135]
	v_lshl_add_u64 v[166:167], v[164:165], 0, s[40:41]
	v_cvt_pk_bf16_f32 v134, v138, v139
	v_cvt_pk_bf16_f32 v135, v140, v141
	v_cvt_pk_bf16_f32 v136, v136, v137
	v_cvt_pk_bf16_f32 v137, v142, v143
	global_store_dwordx4 v[166:167], v[134:137], off offset:256
	s_mov_b32 s50, -1
	s_cbranch_execnz .LBB0_2069
.LBB0_2074:
	s_mov_b32 s32, 1
	s_lshl_b64 s[40:41], s[12:13], 13
	s_add_u32 s40, s72, s40
	v_lshl_or_b32 v0, s60, 7, v178
	s_addc_u32 s41, s73, s41
	v_lshl_add_u64 v[138:139], v[0:1], 2, s[40:41]
	global_load_dwordx4 v[134:137], v[138:139], off offset:16
	global_load_dwordx4 v[142:145], v[138:139], off
	s_mov_b64 s[40:41], 0x1000
	v_lshl_add_u64 v[140:141], v[138:139], 0, s[40:41]
	v_add_co_u32_e32 v138, vcc, s83, v138
	s_mov_b32 s13, 0xc0e00000
	s_nop 0
	v_addc_co_u32_e32 v139, vcc, 0, v139, vcc
	global_load_dwordx4 v[146:149], v[138:139], off
	s_nop 0
	global_load_dwordx4 v[138:141], v[140:141], off offset:16
	v_lshlrev_b32_e32 v0, 1, v0
	v_lshl_add_u32 v0, v162, 11, v0
	v_readlane_b32 s40, v252, 29
	v_readlane_b32 s41, v252, 30
	v_readlane_b32 s42, v252, 31
	v_readlane_b32 s43, v252, 32
	s_mov_b32 s50, s10
	s_waitcnt vmcnt(0)
	v_add_f32_e32 v155, v130, v142
	v_min_f32_e32 v164, 0x40e00000, v155
	v_mul_f32_e32 v155, 0xbfd9db23, v164
	v_mul_f32_e32 v155, 0x3fb8aa3b, v155
	v_exp_f32_e32 v155, v155
	v_add_f32_e32 v161, v98, v146
	v_add_f32_e32 v155, 1.0, v155
	v_rcp_f32_e32 v168, v155
	v_add_f32_e32 v155, v131, v143
	v_min_f32_e32 v165, 0x40e00000, v155
	v_mul_f32_e32 v155, 0xbfd9db23, v165
	v_mul_f32_e32 v155, 0x3fb8aa3b, v155
	v_exp_f32_e32 v155, v155
	v_med3_f32 v166, v161, s13, v222
	v_add_f32_e32 v161, v99, v147
	v_med3_f32 v167, v161, s13, v222
	v_add_f32_e32 v155, 1.0, v155
	v_rcp_f32_e32 v169, v155
	v_pk_add_f32 v[166:167], v[166:167], 1.0 op_sel_hi:[1,0]
	v_add_f32_e32 v155, v132, v144
	v_add_f32_e32 v161, v100, v148
	v_pk_mul_f32 v[164:165], v[164:165], v[168:169]
	v_med3_f32 v168, v161, s13, v222
	v_pk_mul_f32 v[164:165], v[166:167], v[164:165]
	v_min_f32_e32 v166, 0x40e00000, v155
	v_mul_f32_e32 v155, 0xbfd9db23, v166
	v_mul_f32_e32 v155, 0x3fb8aa3b, v155
	v_exp_f32_e32 v155, v155
	v_add_f32_e32 v161, v101, v149
	v_med3_f32 v169, v161, s13, v222
	v_pk_add_f32 v[168:169], v[168:169], 1.0 op_sel_hi:[1,0]
	v_add_f32_e32 v155, 1.0, v155
	v_rcp_f32_e32 v170, v155
	v_add_f32_e32 v155, v133, v145
	v_min_f32_e32 v167, 0x40e00000, v155
	v_mul_f32_e32 v155, 0xbfd9db23, v167
	v_mul_f32_e32 v155, 0x3fb8aa3b, v155
	v_exp_f32_e32 v155, v155
	v_add_f32_e32 v161, v94, v138
	v_cvt_pk_bf16_f32 v164, v164, v165
	v_add_f32_e32 v155, 1.0, v155
	v_rcp_f32_e32 v171, v155
	v_add_f32_e32 v155, v126, v134
	v_pk_mul_f32 v[166:167], v[166:167], v[170:171]
	s_nop 0
	v_pk_mul_f32 v[166:167], v[168:169], v[166:167]
	v_min_f32_e32 v168, 0x40e00000, v155
	v_mul_f32_e32 v155, 0xbfd9db23, v168
	v_mul_f32_e32 v155, 0x3fb8aa3b, v155
	v_exp_f32_e32 v155, v155
	v_med3_f32 v170, v161, s13, v222
	v_add_f32_e32 v161, v95, v139
	v_med3_f32 v171, v161, s13, v222
	v_add_f32_e32 v155, 1.0, v155
	v_rcp_f32_e32 v172, v155
	v_add_f32_e32 v155, v127, v135
	v_min_f32_e32 v169, 0x40e00000, v155
	v_mul_f32_e32 v155, 0xbfd9db23, v169
	v_mul_f32_e32 v155, 0x3fb8aa3b, v155
	v_exp_f32_e32 v155, v155
	v_pk_add_f32 v[170:171], v[170:171], 1.0 op_sel_hi:[1,0]
	v_add_f32_e32 v161, v96, v140
	v_med3_f32 v182, v161, s13, v222
	v_add_f32_e32 v155, 1.0, v155
	v_rcp_f32_e32 v173, v155
	v_add_f32_e32 v155, v128, v136
	v_add_f32_e32 v161, v97, v141
	v_med3_f32 v183, v161, s13, v222
	v_pk_mul_f32 v[168:169], v[168:169], v[172:173]
	v_pk_add_f32 v[182:183], v[182:183], 1.0 op_sel_hi:[1,0]
	v_pk_mul_f32 v[168:169], v[170:171], v[168:169]
	v_min_f32_e32 v170, 0x40e00000, v155
	v_mul_f32_e32 v155, 0xbfd9db23, v170
	v_mul_f32_e32 v155, 0x3fb8aa3b, v155
	v_exp_f32_e32 v155, v155
	v_cvt_pk_bf16_f32 v165, v166, v167
	v_cvt_pk_bf16_f32 v166, v168, v169
	v_add_f32_e32 v161, v90, v146
	v_add_f32_e32 v155, 1.0, v155
	v_rcp_f32_e32 v172, v155
	v_add_f32_e32 v155, v129, v137
	v_min_f32_e32 v171, 0x40e00000, v155
	v_mul_f32_e32 v155, 0xbfd9db23, v171
	v_mul_f32_e32 v155, 0x3fb8aa3b, v155
	v_exp_f32_e32 v155, v155
	s_nop 0
	v_add_f32_e32 v155, 1.0, v155
	v_rcp_f32_e32 v173, v155
	v_add_f32_e32 v155, v122, v142
	v_min_f32_e32 v162, 0x40e00000, v155
	v_mul_f32_e32 v155, 0xbfd9db23, v162
	v_mul_f32_e32 v155, 0x3fb8aa3b, v155
	v_exp_f32_e32 v155, v155
	v_pk_mul_f32 v[170:171], v[170:171], v[172:173]
	v_add_f32_e32 v155, 1.0, v155
	v_pk_mul_f32 v[170:171], v[182:183], v[170:171]
	s_nop 0
	v_cvt_pk_bf16_f32 v167, v170, v171
	buffer_store_dwordx4 v[164:167], v0, s[40:43], 0 offen sc1
	s_nop 1
	v_rcp_f32_e32 v166, v155
	v_add_f32_e32 v155, v123, v143
	v_min_f32_e32 v163, 0x40e00000, v155
	v_mul_f32_e32 v155, 0xbfd9db23, v163
	v_mul_f32_e32 v155, 0x3fb8aa3b, v155
	v_exp_f32_e32 v155, v155
	v_med3_f32 v164, v161, s13, v222
	v_add_f32_e32 v161, v91, v147
	v_med3_f32 v165, v161, s13, v222
	v_add_f32_e32 v155, 1.0, v155
	v_rcp_f32_e32 v167, v155
	v_pk_add_f32 v[164:165], v[164:165], 1.0 op_sel_hi:[1,0]
	v_add_f32_e32 v155, v124, v144
	v_add_f32_e32 v161, v92, v148
	v_pk_mul_f32 v[162:163], v[162:163], v[166:167]
	v_med3_f32 v166, v161, s13, v222
	v_pk_mul_f32 v[162:163], v[164:165], v[162:163]
	v_min_f32_e32 v164, 0x40e00000, v155
	v_mul_f32_e32 v155, 0xbfd9db23, v164
	v_mul_f32_e32 v155, 0x3fb8aa3b, v155
	v_exp_f32_e32 v155, v155
	v_add_f32_e32 v161, v93, v149
	v_med3_f32 v167, v161, s13, v222
	v_pk_add_f32 v[166:167], v[166:167], 1.0 op_sel_hi:[1,0]
	v_add_f32_e32 v155, 1.0, v155
	v_rcp_f32_e32 v168, v155
	v_add_f32_e32 v155, v125, v145
	v_min_f32_e32 v165, 0x40e00000, v155
	v_mul_f32_e32 v155, 0xbfd9db23, v165
	v_mul_f32_e32 v155, 0x3fb8aa3b, v155
	v_exp_f32_e32 v155, v155
	v_add_f32_e32 v161, v86, v138
	v_cvt_pk_bf16_f32 v162, v162, v163
	v_add_f32_e32 v155, 1.0, v155
	v_rcp_f32_e32 v169, v155
	v_add_f32_e32 v155, v118, v134
	v_pk_mul_f32 v[164:165], v[164:165], v[168:169]
	s_nop 0
	v_pk_mul_f32 v[164:165], v[166:167], v[164:165]
	v_min_f32_e32 v166, 0x40e00000, v155
	v_mul_f32_e32 v155, 0xbfd9db23, v166
	v_mul_f32_e32 v155, 0x3fb8aa3b, v155
	v_exp_f32_e32 v155, v155
	v_med3_f32 v168, v161, s13, v222
	v_add_f32_e32 v161, v87, v139
	v_med3_f32 v169, v161, s13, v222
	v_add_f32_e32 v155, 1.0, v155
	v_rcp_f32_e32 v170, v155
	v_add_f32_e32 v155, v119, v135
	v_min_f32_e32 v167, 0x40e00000, v155
	v_mul_f32_e32 v155, 0xbfd9db23, v167
	v_mul_f32_e32 v155, 0x3fb8aa3b, v155
	v_exp_f32_e32 v155, v155
	v_pk_add_f32 v[168:169], v[168:169], 1.0 op_sel_hi:[1,0]
	v_add_f32_e32 v161, v88, v140
	v_cvt_pk_bf16_f32 v163, v164, v165
	v_add_f32_e32 v155, 1.0, v155
	v_rcp_f32_e32 v171, v155
	v_add_f32_e32 v155, v120, v136
	v_pk_mul_f32 v[166:167], v[166:167], v[170:171]
	s_nop 0
	v_pk_mul_f32 v[166:167], v[168:169], v[166:167]
	v_min_f32_e32 v168, 0x40e00000, v155
	v_mul_f32_e32 v155, 0xbfd9db23, v168
	v_mul_f32_e32 v155, 0x3fb8aa3b, v155
	v_exp_f32_e32 v155, v155
	v_med3_f32 v170, v161, s13, v222
	v_add_f32_e32 v161, v89, v141
	v_med3_f32 v171, v161, s13, v222
	v_add_f32_e32 v155, 1.0, v155
	v_rcp_f32_e32 v172, v155
	v_add_f32_e32 v155, v121, v137
	v_min_f32_e32 v169, 0x40e00000, v155
	v_mul_f32_e32 v155, 0xbfd9db23, v169
	v_mul_f32_e32 v155, 0x3fb8aa3b, v155
	v_exp_f32_e32 v155, v155
	v_pk_add_f32 v[170:171], v[170:171], 1.0 op_sel_hi:[1,0]
	v_cvt_pk_bf16_f32 v164, v166, v167
	v_add_f32_e32 v161, v82, v146
	v_add_f32_e32 v155, 1.0, v155
	v_rcp_f32_e32 v173, v155
	v_add_u32_e32 v155, 0x8000, v0
	v_pk_mul_f32 v[168:169], v[168:169], v[172:173]
	s_nop 0
	v_pk_mul_f32 v[168:169], v[170:171], v[168:169]
	s_nop 0
	v_cvt_pk_bf16_f32 v165, v168, v169
	buffer_store_dwordx4 v[162:165], v155, s[40:43], 0 offen sc1
	v_add_f32_e32 v155, v114, v142
	s_nop 0
	v_min_f32_e32 v162, 0x40e00000, v155
	v_mul_f32_e32 v155, 0xbfd9db23, v162
	v_mul_f32_e32 v155, 0x3fb8aa3b, v155
	v_exp_f32_e32 v155, v155
	v_med3_f32 v164, v161, s13, v222
	v_add_f32_e32 v161, v83, v147
	v_med3_f32 v165, v161, s13, v222
	v_add_f32_e32 v155, 1.0, v155
	v_rcp_f32_e32 v166, v155
	v_add_f32_e32 v155, v115, v143
	v_min_f32_e32 v163, 0x40e00000, v155
	v_mul_f32_e32 v155, 0xbfd9db23, v163
	v_mul_f32_e32 v155, 0x3fb8aa3b, v155
	v_exp_f32_e32 v155, v155
	v_pk_add_f32 v[164:165], v[164:165], 1.0 op_sel_hi:[1,0]
	v_add_f32_e32 v161, v84, v148
	v_add_f32_e32 v155, 1.0, v155
	v_rcp_f32_e32 v167, v155
	v_add_f32_e32 v155, v116, v144
	v_pk_mul_f32 v[162:163], v[162:163], v[166:167]
	s_nop 0
	v_pk_mul_f32 v[162:163], v[164:165], v[162:163]
	v_min_f32_e32 v164, 0x40e00000, v155
	v_mul_f32_e32 v155, 0xbfd9db23, v164
	v_mul_f32_e32 v155, 0x3fb8aa3b, v155
	v_exp_f32_e32 v155, v155
	v_med3_f32 v166, v161, s13, v222
	v_add_f32_e32 v161, v85, v149
	v_med3_f32 v167, v161, s13, v222
	v_add_f32_e32 v155, 1.0, v155
	v_rcp_f32_e32 v168, v155
	v_add_f32_e32 v155, v117, v145
	v_min_f32_e32 v165, 0x40e00000, v155
	v_mul_f32_e32 v155, 0xbfd9db23, v165
	v_mul_f32_e32 v155, 0x3fb8aa3b, v155
	v_exp_f32_e32 v155, v155
	v_pk_add_f32 v[166:167], v[166:167], 1.0 op_sel_hi:[1,0]
	v_add_f32_e32 v161, v78, v138
	v_cvt_pk_bf16_f32 v162, v162, v163
	v_add_f32_e32 v155, 1.0, v155
	v_rcp_f32_e32 v169, v155
	v_add_f32_e32 v155, v110, v134
	v_pk_mul_f32 v[164:165], v[164:165], v[168:169]
	s_nop 0
	v_pk_mul_f32 v[164:165], v[166:167], v[164:165]
	v_min_f32_e32 v166, 0x40e00000, v155
	v_mul_f32_e32 v155, 0xbfd9db23, v166
	v_mul_f32_e32 v155, 0x3fb8aa3b, v155
	v_exp_f32_e32 v155, v155
	v_med3_f32 v168, v161, s13, v222
	v_add_f32_e32 v161, v79, v139
	v_med3_f32 v169, v161, s13, v222
	v_add_f32_e32 v155, 1.0, v155
	v_rcp_f32_e32 v170, v155
	v_add_f32_e32 v155, v111, v135
	v_min_f32_e32 v167, 0x40e00000, v155
	v_mul_f32_e32 v155, 0xbfd9db23, v167
	v_mul_f32_e32 v155, 0x3fb8aa3b, v155
	v_exp_f32_e32 v155, v155
	v_pk_add_f32 v[168:169], v[168:169], 1.0 op_sel_hi:[1,0]
	v_add_f32_e32 v161, v80, v140
	v_cvt_pk_bf16_f32 v163, v164, v165
	v_add_f32_e32 v155, 1.0, v155
	v_rcp_f32_e32 v171, v155
	v_add_f32_e32 v155, v112, v136
	v_pk_mul_f32 v[166:167], v[166:167], v[170:171]
	s_nop 0
	v_pk_mul_f32 v[166:167], v[168:169], v[166:167]
	v_min_f32_e32 v168, 0x40e00000, v155
	v_mul_f32_e32 v155, 0xbfd9db23, v168
	v_mul_f32_e32 v155, 0x3fb8aa3b, v155
	v_exp_f32_e32 v155, v155
	v_med3_f32 v170, v161, s13, v222
	v_add_f32_e32 v161, v81, v141
	v_med3_f32 v171, v161, s13, v222
	v_add_f32_e32 v155, 1.0, v155
	v_rcp_f32_e32 v172, v155
	v_add_f32_e32 v155, v113, v137
	v_min_f32_e32 v169, 0x40e00000, v155
	v_mul_f32_e32 v155, 0xbfd9db23, v169
	v_mul_f32_e32 v155, 0x3fb8aa3b, v155
	v_exp_f32_e32 v155, v155
	v_pk_add_f32 v[170:171], v[170:171], 1.0 op_sel_hi:[1,0]
	v_cvt_pk_bf16_f32 v164, v166, v167
	v_add_f32_e32 v161, v74, v146
	v_add_f32_e32 v155, 1.0, v155
	v_rcp_f32_e32 v173, v155
	v_add_u32_e32 v155, 0x10000, v0
	v_pk_mul_f32 v[168:169], v[168:169], v[172:173]
	s_nop 0
	v_pk_mul_f32 v[168:169], v[170:171], v[168:169]
	s_nop 0
	v_cvt_pk_bf16_f32 v165, v168, v169
	buffer_store_dwordx4 v[162:165], v155, s[40:43], 0 offen sc1
	v_add_f32_e32 v155, v106, v142
	s_nop 0
	v_min_f32_e32 v162, 0x40e00000, v155
	v_mul_f32_e32 v155, 0xbfd9db23, v162
	v_mul_f32_e32 v155, 0x3fb8aa3b, v155
	v_exp_f32_e32 v155, v155
	v_med3_f32 v164, v161, s13, v222
	v_add_f32_e32 v161, v75, v147
	v_med3_f32 v165, v161, s13, v222
	v_add_f32_e32 v155, 1.0, v155
	v_rcp_f32_e32 v166, v155
	v_add_f32_e32 v155, v107, v143
	v_min_f32_e32 v163, 0x40e00000, v155
	v_mul_f32_e32 v155, 0xbfd9db23, v163
	v_mul_f32_e32 v155, 0x3fb8aa3b, v155
	v_exp_f32_e32 v155, v155
	v_pk_add_f32 v[164:165], v[164:165], 1.0 op_sel_hi:[1,0]
	v_add_f32_e32 v161, v76, v148
	v_add_f32_e32 v155, 1.0, v155
	v_rcp_f32_e32 v167, v155
	v_add_f32_e32 v155, v108, v144
	v_pk_mul_f32 v[162:163], v[162:163], v[166:167]
	s_nop 0
	v_pk_mul_f32 v[162:163], v[164:165], v[162:163]
	v_min_f32_e32 v164, 0x40e00000, v155
	v_mul_f32_e32 v155, 0xbfd9db23, v164
	v_mul_f32_e32 v155, 0x3fb8aa3b, v155
	v_exp_f32_e32 v155, v155
	v_med3_f32 v166, v161, s13, v222
	v_add_f32_e32 v161, v77, v149
	v_med3_f32 v167, v161, s13, v222
	v_add_f32_e32 v155, 1.0, v155
	v_rcp_f32_e32 v168, v155
	v_add_f32_e32 v155, v109, v145
	v_min_f32_e32 v165, 0x40e00000, v155
	v_mul_f32_e32 v155, 0xbfd9db23, v165
	v_mul_f32_e32 v155, 0x3fb8aa3b, v155
	v_exp_f32_e32 v155, v155
	v_pk_add_f32 v[166:167], v[166:167], 1.0 op_sel_hi:[1,0]
	v_add_f32_e32 v161, v70, v138
	v_cvt_pk_bf16_f32 v162, v162, v163
	v_add_f32_e32 v155, 1.0, v155
	v_rcp_f32_e32 v169, v155
	v_add_f32_e32 v155, v102, v134
	v_pk_mul_f32 v[164:165], v[164:165], v[168:169]
	s_nop 0
	v_pk_mul_f32 v[164:165], v[166:167], v[164:165]
	v_min_f32_e32 v166, 0x40e00000, v155
	v_mul_f32_e32 v155, 0xbfd9db23, v166
	v_mul_f32_e32 v155, 0x3fb8aa3b, v155
	v_exp_f32_e32 v155, v155
	v_med3_f32 v168, v161, s13, v222
	v_add_f32_e32 v161, v71, v139
	v_med3_f32 v169, v161, s13, v222
	v_add_f32_e32 v155, 1.0, v155
	v_rcp_f32_e32 v170, v155
	v_add_f32_e32 v155, v103, v135
	v_min_f32_e32 v167, 0x40e00000, v155
	v_mul_f32_e32 v155, 0xbfd9db23, v167
	v_mul_f32_e32 v155, 0x3fb8aa3b, v155
	v_exp_f32_e32 v155, v155
	v_pk_add_f32 v[168:169], v[168:169], 1.0 op_sel_hi:[1,0]
	v_add_f32_e32 v161, v72, v140
	v_cvt_pk_bf16_f32 v163, v164, v165
	v_add_f32_e32 v155, 1.0, v155
	v_rcp_f32_e32 v171, v155
	v_add_f32_e32 v155, v104, v136
	v_pk_mul_f32 v[166:167], v[166:167], v[170:171]
	s_nop 0
	v_pk_mul_f32 v[166:167], v[168:169], v[166:167]
	v_min_f32_e32 v168, 0x40e00000, v155
	v_mul_f32_e32 v155, 0xbfd9db23, v168
	v_mul_f32_e32 v155, 0x3fb8aa3b, v155
	v_exp_f32_e32 v155, v155
	v_med3_f32 v170, v161, s13, v222
	v_add_f32_e32 v161, v73, v141
	v_med3_f32 v171, v161, s13, v222
	v_add_f32_e32 v155, 1.0, v155
	v_rcp_f32_e32 v172, v155
	v_add_f32_e32 v155, v105, v137
	v_min_f32_e32 v169, 0x40e00000, v155
	v_mul_f32_e32 v155, 0xbfd9db23, v169
	v_mul_f32_e32 v155, 0x3fb8aa3b, v155
	v_exp_f32_e32 v155, v155
	v_pk_add_f32 v[170:171], v[170:171], 1.0 op_sel_hi:[1,0]
	v_cvt_pk_bf16_f32 v164, v166, v167
	v_add_f32_e32 v161, v30, v146
	v_add_f32_e32 v155, 1.0, v155
	v_rcp_f32_e32 v173, v155
	v_add_u32_e32 v155, 0x18000, v0
	v_pk_mul_f32 v[168:169], v[168:169], v[172:173]
	s_nop 0
	v_pk_mul_f32 v[168:169], v[170:171], v[168:169]
	s_nop 0
	v_cvt_pk_bf16_f32 v165, v168, v169
	buffer_store_dwordx4 v[162:165], v155, s[40:43], 0 offen sc1
	v_add_f32_e32 v155, v66, v142
	s_nop 0
	v_min_f32_e32 v162, 0x40e00000, v155
	v_mul_f32_e32 v155, 0xbfd9db23, v162
	v_mul_f32_e32 v155, 0x3fb8aa3b, v155
	v_exp_f32_e32 v155, v155
	v_med3_f32 v164, v161, s13, v222
	v_add_f32_e32 v161, v31, v147
	v_med3_f32 v165, v161, s13, v222
	v_add_f32_e32 v155, 1.0, v155
	v_rcp_f32_e32 v166, v155
	v_add_f32_e32 v155, v67, v143
	v_min_f32_e32 v163, 0x40e00000, v155
	v_mul_f32_e32 v155, 0xbfd9db23, v163
	v_mul_f32_e32 v155, 0x3fb8aa3b, v155
	v_exp_f32_e32 v155, v155
	v_pk_add_f32 v[164:165], v[164:165], 1.0 op_sel_hi:[1,0]
	v_add_f32_e32 v161, v32, v148
	v_add_f32_e32 v155, 1.0, v155
	v_rcp_f32_e32 v167, v155
	v_add_f32_e32 v155, v68, v144
	v_pk_mul_f32 v[162:163], v[162:163], v[166:167]
	s_nop 0
	v_pk_mul_f32 v[162:163], v[164:165], v[162:163]
	v_min_f32_e32 v164, 0x40e00000, v155
	v_mul_f32_e32 v155, 0xbfd9db23, v164
	v_mul_f32_e32 v155, 0x3fb8aa3b, v155
	v_exp_f32_e32 v155, v155
	v_med3_f32 v166, v161, s13, v222
	v_add_f32_e32 v161, v33, v149
	v_med3_f32 v167, v161, s13, v222
	v_add_f32_e32 v155, 1.0, v155
	v_rcp_f32_e32 v168, v155
	v_add_f32_e32 v155, v69, v145
	v_min_f32_e32 v165, 0x40e00000, v155
	v_mul_f32_e32 v155, 0xbfd9db23, v165
	v_mul_f32_e32 v155, 0x3fb8aa3b, v155
	v_exp_f32_e32 v155, v155
	v_pk_add_f32 v[166:167], v[166:167], 1.0 op_sel_hi:[1,0]
	v_add_f32_e32 v161, v26, v138
	v_cvt_pk_bf16_f32 v162, v162, v163
	v_add_f32_e32 v155, 1.0, v155
	v_rcp_f32_e32 v169, v155
	v_add_f32_e32 v155, v62, v134
	v_pk_mul_f32 v[164:165], v[164:165], v[168:169]
	s_nop 0
	v_pk_mul_f32 v[164:165], v[166:167], v[164:165]
	v_min_f32_e32 v166, 0x40e00000, v155
	v_mul_f32_e32 v155, 0xbfd9db23, v166
	v_mul_f32_e32 v155, 0x3fb8aa3b, v155
	v_exp_f32_e32 v155, v155
	v_med3_f32 v168, v161, s13, v222
	v_add_f32_e32 v161, v27, v139
	v_med3_f32 v169, v161, s13, v222
	v_add_f32_e32 v155, 1.0, v155
	v_rcp_f32_e32 v170, v155
	v_add_f32_e32 v155, v63, v135
	v_min_f32_e32 v167, 0x40e00000, v155
	v_mul_f32_e32 v155, 0xbfd9db23, v167
	v_mul_f32_e32 v155, 0x3fb8aa3b, v155
	v_exp_f32_e32 v155, v155
	v_pk_add_f32 v[168:169], v[168:169], 1.0 op_sel_hi:[1,0]
	v_add_f32_e32 v161, v28, v140
	v_cvt_pk_bf16_f32 v163, v164, v165
	v_add_f32_e32 v155, 1.0, v155
	v_rcp_f32_e32 v171, v155
	v_add_f32_e32 v155, v64, v136
	v_pk_mul_f32 v[166:167], v[166:167], v[170:171]
	s_nop 0
	v_pk_mul_f32 v[166:167], v[168:169], v[166:167]
	v_min_f32_e32 v168, 0x40e00000, v155
	v_mul_f32_e32 v155, 0xbfd9db23, v168
	v_mul_f32_e32 v155, 0x3fb8aa3b, v155
	v_exp_f32_e32 v155, v155
	v_med3_f32 v170, v161, s13, v222
	v_add_f32_e32 v161, v29, v141
	v_med3_f32 v171, v161, s13, v222
	v_add_f32_e32 v155, 1.0, v155
	v_rcp_f32_e32 v172, v155
	v_add_f32_e32 v155, v65, v137
	v_min_f32_e32 v169, 0x40e00000, v155
	v_mul_f32_e32 v155, 0xbfd9db23, v169
	v_mul_f32_e32 v155, 0x3fb8aa3b, v155
	v_exp_f32_e32 v155, v155
	v_pk_add_f32 v[170:171], v[170:171], 1.0 op_sel_hi:[1,0]
	v_cvt_pk_bf16_f32 v164, v166, v167
	v_add_f32_e32 v161, v22, v146
	v_add_f32_e32 v155, 1.0, v155
	v_rcp_f32_e32 v173, v155
	v_add_u32_e32 v155, 0x40000, v0
	v_pk_mul_f32 v[168:169], v[168:169], v[172:173]
	s_nop 0
	v_pk_mul_f32 v[168:169], v[170:171], v[168:169]
	s_nop 0
	v_cvt_pk_bf16_f32 v165, v168, v169
	buffer_store_dwordx4 v[162:165], v155, s[40:43], 0 offen sc1
	v_add_f32_e32 v155, v58, v142
	s_nop 0
	v_min_f32_e32 v162, 0x40e00000, v155
	v_mul_f32_e32 v155, 0xbfd9db23, v162
	v_mul_f32_e32 v155, 0x3fb8aa3b, v155
	v_exp_f32_e32 v155, v155
	v_med3_f32 v164, v161, s13, v222
	v_add_f32_e32 v161, v23, v147
	v_med3_f32 v165, v161, s13, v222
	v_add_f32_e32 v155, 1.0, v155
	v_rcp_f32_e32 v166, v155
	v_add_f32_e32 v155, v59, v143
	v_min_f32_e32 v163, 0x40e00000, v155
	v_mul_f32_e32 v155, 0xbfd9db23, v163
	v_mul_f32_e32 v155, 0x3fb8aa3b, v155
	v_exp_f32_e32 v155, v155
	v_pk_add_f32 v[164:165], v[164:165], 1.0 op_sel_hi:[1,0]
	v_add_f32_e32 v161, v24, v148
	v_add_f32_e32 v155, 1.0, v155
	v_rcp_f32_e32 v167, v155
	v_add_f32_e32 v155, v60, v144
	v_pk_mul_f32 v[162:163], v[162:163], v[166:167]
	s_nop 0
	v_pk_mul_f32 v[162:163], v[164:165], v[162:163]
	v_min_f32_e32 v164, 0x40e00000, v155
	v_mul_f32_e32 v155, 0xbfd9db23, v164
	v_mul_f32_e32 v155, 0x3fb8aa3b, v155
	v_exp_f32_e32 v155, v155
	v_med3_f32 v166, v161, s13, v222
	v_add_f32_e32 v161, v25, v149
	v_med3_f32 v167, v161, s13, v222
	v_add_f32_e32 v155, 1.0, v155
	v_rcp_f32_e32 v168, v155
	v_add_f32_e32 v155, v61, v145
	v_min_f32_e32 v165, 0x40e00000, v155
	v_mul_f32_e32 v155, 0xbfd9db23, v165
	v_mul_f32_e32 v155, 0x3fb8aa3b, v155
	v_exp_f32_e32 v155, v155
	v_pk_add_f32 v[166:167], v[166:167], 1.0 op_sel_hi:[1,0]
	v_add_f32_e32 v161, v18, v138
	v_cvt_pk_bf16_f32 v162, v162, v163
	v_add_f32_e32 v155, 1.0, v155
	v_rcp_f32_e32 v169, v155
	v_add_f32_e32 v155, v54, v134
	v_pk_mul_f32 v[164:165], v[164:165], v[168:169]
	s_nop 0
	v_pk_mul_f32 v[164:165], v[166:167], v[164:165]
	v_min_f32_e32 v166, 0x40e00000, v155
	v_mul_f32_e32 v155, 0xbfd9db23, v166
	v_mul_f32_e32 v155, 0x3fb8aa3b, v155
	v_exp_f32_e32 v155, v155
	v_med3_f32 v168, v161, s13, v222
	v_add_f32_e32 v161, v19, v139
	v_med3_f32 v169, v161, s13, v222
	v_add_f32_e32 v155, 1.0, v155
	v_rcp_f32_e32 v170, v155
	v_add_f32_e32 v155, v55, v135
	v_min_f32_e32 v167, 0x40e00000, v155
	v_mul_f32_e32 v155, 0xbfd9db23, v167
	v_mul_f32_e32 v155, 0x3fb8aa3b, v155
	v_exp_f32_e32 v155, v155
	v_pk_add_f32 v[168:169], v[168:169], 1.0 op_sel_hi:[1,0]
	v_add_f32_e32 v161, v20, v140
	v_cvt_pk_bf16_f32 v163, v164, v165
	v_add_f32_e32 v155, 1.0, v155
	v_rcp_f32_e32 v171, v155
	v_add_f32_e32 v155, v56, v136
	v_pk_mul_f32 v[166:167], v[166:167], v[170:171]
	s_nop 0
	v_pk_mul_f32 v[166:167], v[168:169], v[166:167]
	v_min_f32_e32 v168, 0x40e00000, v155
	v_mul_f32_e32 v155, 0xbfd9db23, v168
	v_mul_f32_e32 v155, 0x3fb8aa3b, v155
	v_exp_f32_e32 v155, v155
	v_med3_f32 v170, v161, s13, v222
	v_add_f32_e32 v161, v21, v141
	v_med3_f32 v171, v161, s13, v222
	v_add_f32_e32 v155, 1.0, v155
	v_rcp_f32_e32 v172, v155
	v_add_f32_e32 v155, v57, v137
	v_min_f32_e32 v169, 0x40e00000, v155
	v_mul_f32_e32 v155, 0xbfd9db23, v169
	v_mul_f32_e32 v155, 0x3fb8aa3b, v155
	v_exp_f32_e32 v155, v155
	v_pk_add_f32 v[170:171], v[170:171], 1.0 op_sel_hi:[1,0]
	v_cvt_pk_bf16_f32 v164, v166, v167
	v_add_f32_e32 v161, v14, v146
	v_add_f32_e32 v155, 1.0, v155
	v_rcp_f32_e32 v173, v155
	v_add_u32_e32 v155, 0x48000, v0
	v_add_f32_e32 v146, v6, v146
	v_med3_f32 v146, v146, s13, v222
	v_pk_mul_f32 v[168:169], v[168:169], v[172:173]
	s_nop 0
	v_pk_mul_f32 v[168:169], v[170:171], v[168:169]
	s_nop 0
	v_cvt_pk_bf16_f32 v165, v168, v169
	buffer_store_dwordx4 v[162:165], v155, s[40:43], 0 offen sc1
	v_add_f32_e32 v155, v50, v142
	v_add_f32_e32 v142, v42, v142
	v_min_f32_e32 v162, 0x40e00000, v155
	v_mul_f32_e32 v155, 0xbfd9db23, v162
	v_mul_f32_e32 v155, 0x3fb8aa3b, v155
	v_exp_f32_e32 v155, v155
	v_med3_f32 v164, v161, s13, v222
	v_add_f32_e32 v161, v15, v147
	v_med3_f32 v165, v161, s13, v222
	v_add_f32_e32 v155, 1.0, v155
	v_rcp_f32_e32 v166, v155
	v_add_f32_e32 v155, v51, v143
	v_min_f32_e32 v163, 0x40e00000, v155
	v_mul_f32_e32 v155, 0xbfd9db23, v163
	v_mul_f32_e32 v155, 0x3fb8aa3b, v155
	v_exp_f32_e32 v155, v155
	v_pk_add_f32 v[164:165], v[164:165], 1.0 op_sel_hi:[1,0]
	v_add_f32_e32 v161, v16, v148
	v_min_f32_e32 v142, 0x40e00000, v142
	v_add_f32_e32 v155, 1.0, v155
	v_rcp_f32_e32 v167, v155
	v_add_f32_e32 v155, v52, v144
	v_add_f32_e32 v143, v43, v143
	v_min_f32_e32 v143, 0x40e00000, v143
	v_pk_mul_f32 v[162:163], v[162:163], v[166:167]
	v_med3_f32 v166, v161, s13, v222
	v_pk_mul_f32 v[162:163], v[164:165], v[162:163]
	v_min_f32_e32 v164, 0x40e00000, v155
	v_mul_f32_e32 v155, 0xbfd9db23, v164
	v_mul_f32_e32 v155, 0x3fb8aa3b, v155
	v_exp_f32_e32 v155, v155
	v_add_f32_e32 v161, v17, v149
	v_med3_f32 v167, v161, s13, v222
	v_pk_add_f32 v[166:167], v[166:167], 1.0 op_sel_hi:[1,0]
	v_add_f32_e32 v155, 1.0, v155
	v_rcp_f32_e32 v168, v155
	v_add_f32_e32 v155, v53, v145
	v_min_f32_e32 v165, 0x40e00000, v155
	v_mul_f32_e32 v155, 0xbfd9db23, v165
	v_mul_f32_e32 v155, 0x3fb8aa3b, v155
	v_exp_f32_e32 v155, v155
	v_add_f32_e32 v161, v10, v138
	v_cvt_pk_bf16_f32 v162, v162, v163
	v_add_f32_e32 v147, v7, v147
	v_add_f32_e32 v155, 1.0, v155
	v_rcp_f32_e32 v169, v155
	v_add_f32_e32 v155, v46, v134
	v_med3_f32 v147, v147, s13, v222
	v_add_f32_e32 v144, v44, v144
	v_pk_mul_f32 v[164:165], v[164:165], v[168:169]
	v_med3_f32 v168, v161, s13, v222
	v_pk_mul_f32 v[164:165], v[166:167], v[164:165]
	v_min_f32_e32 v166, 0x40e00000, v155
	v_mul_f32_e32 v155, 0xbfd9db23, v166
	v_mul_f32_e32 v155, 0x3fb8aa3b, v155
	v_exp_f32_e32 v155, v155
	v_add_f32_e32 v161, v11, v139
	v_med3_f32 v169, v161, s13, v222
	v_pk_add_f32 v[168:169], v[168:169], 1.0 op_sel_hi:[1,0]
	v_add_f32_e32 v155, 1.0, v155
	v_rcp_f32_e32 v170, v155
	v_add_f32_e32 v155, v47, v135
	v_min_f32_e32 v167, 0x40e00000, v155
	v_mul_f32_e32 v155, 0xbfd9db23, v167
	v_mul_f32_e32 v155, 0x3fb8aa3b, v155
	v_exp_f32_e32 v155, v155
	v_add_f32_e32 v161, v12, v140
	v_cvt_pk_bf16_f32 v163, v164, v165
	v_pk_add_f32 v[146:147], v[146:147], 1.0 op_sel_hi:[1,0]
	v_add_f32_e32 v155, 1.0, v155
	v_rcp_f32_e32 v171, v155
	v_add_f32_e32 v155, v48, v136
	v_min_f32_e32 v144, 0x40e00000, v144
	v_add_f32_e32 v145, v45, v145
	v_pk_mul_f32 v[166:167], v[166:167], v[170:171]
	v_med3_f32 v170, v161, s13, v222
	v_pk_mul_f32 v[166:167], v[168:169], v[166:167]
	v_min_f32_e32 v168, 0x40e00000, v155
	v_mul_f32_e32 v155, 0xbfd9db23, v168
	v_mul_f32_e32 v155, 0x3fb8aa3b, v155
	v_exp_f32_e32 v155, v155
	v_add_f32_e32 v161, v13, v141
	v_med3_f32 v171, v161, s13, v222
	v_pk_add_f32 v[170:171], v[170:171], 1.0 op_sel_hi:[1,0]
	v_add_f32_e32 v155, 1.0, v155
	v_rcp_f32_e32 v172, v155
	v_add_f32_e32 v155, v49, v137
	v_min_f32_e32 v169, 0x40e00000, v155
	v_mul_f32_e32 v155, 0xbfd9db23, v169
	v_mul_f32_e32 v155, 0x3fb8aa3b, v155
	v_exp_f32_e32 v155, v155
	v_cvt_pk_bf16_f32 v164, v166, v167
	v_min_f32_e32 v145, 0x40e00000, v145
	v_add_f32_e32 v134, v38, v134
	v_add_f32_e32 v155, 1.0, v155
	v_rcp_f32_e32 v173, v155
	v_add_u32_e32 v155, 0x50000, v0
	v_add_f32_e32 v135, v39, v135
	v_min_f32_e32 v134, 0x40e00000, v134
	v_pk_mul_f32 v[168:169], v[168:169], v[172:173]
	v_min_f32_e32 v135, 0x40e00000, v135
	v_pk_mul_f32 v[168:169], v[170:171], v[168:169]
	v_add_f32_e32 v138, v2, v138
	v_cvt_pk_bf16_f32 v165, v168, v169
	buffer_store_dwordx4 v[162:165], v155, s[40:43], 0 offen sc1
	v_mul_f32_e32 v155, 0xbfd9db23, v142
	v_mul_f32_e32 v155, 0x3fb8aa3b, v155
	v_exp_f32_e32 v155, v155
	v_add_f32_e32 v139, v3, v139
	v_med3_f32 v138, v138, s13, v222
	v_med3_f32 v139, v139, s13, v222
	v_add_f32_e32 v155, 1.0, v155
	v_rcp_f32_e32 v162, v155
	v_mul_f32_e32 v155, 0xbfd9db23, v143
	v_mul_f32_e32 v155, 0x3fb8aa3b, v155
	v_exp_f32_e32 v155, v155
	v_pk_add_f32 v[138:139], v[138:139], 1.0 op_sel_hi:[1,0]
	v_add_u32_e32 v0, 0x58000, v0
	v_add_f32_e32 v155, 1.0, v155
	v_rcp_f32_e32 v163, v155
	s_nop 0
	v_pk_mul_f32 v[142:143], v[142:143], v[162:163]
	s_nop 0
	v_pk_mul_f32 v[142:143], v[146:147], v[142:143]
	v_mul_f32_e32 v147, 0xbfd9db23, v144
	v_mul_f32_e32 v147, 0x3fb8aa3b, v147
	v_exp_f32_e32 v147, v147
	v_add_f32_e32 v146, v8, v148
	v_med3_f32 v146, v146, s13, v222
	v_add_f32_e32 v147, 1.0, v147
	v_rcp_f32_e32 v148, v147
	v_add_f32_e32 v147, v9, v149
	v_mul_f32_e32 v149, 0xbfd9db23, v145
	v_mul_f32_e32 v149, 0x3fb8aa3b, v149
	v_exp_f32_e32 v149, v149
	v_med3_f32 v147, v147, s13, v222
	v_pk_add_f32 v[146:147], v[146:147], 1.0 op_sel_hi:[1,0]
	v_add_f32_e32 v149, 1.0, v149
	v_rcp_f32_e32 v149, v149
	s_nop 0
	v_pk_mul_f32 v[144:145], v[144:145], v[148:149]
	s_nop 0
	v_pk_mul_f32 v[144:145], v[146:147], v[144:145]
	v_mul_f32_e32 v146, 0xbfd9db23, v134
	v_mul_f32_e32 v147, 0xbfd9db23, v135
	v_mul_f32_e32 v146, 0x3fb8aa3b, v146
	v_mul_f32_e32 v147, 0x3fb8aa3b, v147
	v_exp_f32_e32 v146, v146
	v_exp_f32_e32 v147, v147
	v_add_f32_e32 v146, 1.0, v146
	v_add_f32_e32 v147, 1.0, v147
	v_rcp_f32_e32 v146, v146
	v_rcp_f32_e32 v147, v147
	s_nop 0
	v_pk_mul_f32 v[134:135], v[134:135], v[146:147]
	s_nop 0
	v_pk_mul_f32 v[138:139], v[138:139], v[134:135]
	v_add_f32_e32 v134, v40, v136
	v_add_f32_e32 v135, v4, v140
	v_min_f32_e32 v134, 0x40e00000, v134
	v_med3_f32 v136, v135, s13, v222
	v_mul_f32_e32 v135, 0xbfd9db23, v134
	v_mul_f32_e32 v135, 0x3fb8aa3b, v135
	v_exp_f32_e32 v135, v135
	s_nop 0
	v_add_f32_e32 v135, 1.0, v135
	v_rcp_f32_e32 v140, v135
	v_add_f32_e32 v135, v41, v137
	v_min_f32_e32 v135, 0x40e00000, v135
	v_add_f32_e32 v137, v5, v141
	v_mul_f32_e32 v141, 0xbfd9db23, v135
	v_mul_f32_e32 v141, 0x3fb8aa3b, v141
	v_exp_f32_e32 v141, v141
	v_med3_f32 v137, v137, s13, v222
	v_pk_add_f32 v[136:137], v[136:137], 1.0 op_sel_hi:[1,0]
	v_add_f32_e32 v141, 1.0, v141
	v_rcp_f32_e32 v141, v141
	s_nop 0
	v_pk_mul_f32 v[134:135], v[134:135], v[140:141]
	s_nop 0
	v_pk_mul_f32 v[140:141], v[136:137], v[134:135]
	v_cvt_pk_bf16_f32 v134, v142, v143
	v_cvt_pk_bf16_f32 v135, v144, v145
	v_cvt_pk_bf16_f32 v136, v138, v139
	v_cvt_pk_bf16_f32 v137, v140, v141
	buffer_store_dwordx4 v[134:137], v0, s[40:43], 0 offen sc1
	s_add_u32 s42, s29, 0xffffff00
	s_addc_u32 s43, s31, -1
	s_and_b64 vcc, exec, s[0:1]
	s_cbranch_vccz .LBB0_2070

.LBB0_2076:
	s_movk_i32 s40, 0x90
	v_readlane_b32 s41, v253, 59
	s_movk_i32 s43, 0xa000
	s_andn2_b64 vcc, exec, s[36:37]
	s_cbranch_vccz .LBB0_2081
	v_mov_b32_e32 v160, v187
	v_mov_b32_e32 v154, v181
	v_mov_b32_e32 v156, v186
	v_mov_b32_e32 v158, v188
	s_mov_b64 s[52:53], s[38:39]
	s_mov_b64 s[34:35], s[2:3]
	s_mov_b32 s81, s82
	s_branch .LBB0_2031
.LBB0_2081:
	s_waitcnt vmcnt(0)
	s_cmp_gt_i32 s50, -1
	s_cselect_b64 s[0:1], -1, 0
	s_and_b64 s[2:3], s[4:5], s[0:1]
	s_barrier
	s_and_saveexec_b64 s[0:1], s[2:3]
	s_cbranch_execz .LBB0_2084
	s_mov_b64 s[2:3], exec
	v_mbcnt_lo_u32_b32 v0, s2, 0
	v_mbcnt_hi_u32_b32 v0, s3, v0
	v_cmp_eq_u32_e32 vcc, 0, v0
	s_and_b64 s[4:5], exec, vcc
	s_mov_b64 exec, s[4:5]
	s_cbranch_execz .LBB0_2084
	v_readlane_b32 s4, v253, 54
	v_readlane_b32 s5, v253, 55
	s_mov_b32 s51, s4
	s_lshl_b64 s[4:5], s[50:51], 2
	s_add_u32 s4, s14, s4
	s_addc_u32 s5, s15, s5
	s_bcnt1_i32_b64 s2, s[2:3]
	v_mov_b32_e32 v0, s2
	global_atomic_add v1, v0, s[4:5]
	v_readlane_b32 s6, v253, 56
	v_readlane_b32 s7, v253, 57
